# P0: odd workgroups run the HBM-bound expert conversion first and the table/adaLN/small-weight sections after it (even ones keep the order), overlapping the two kinds of work
# speedup vs baseline: 1.0746x; 1.0142x over previous
.LBB0_15:
	v_writelane_b32 v253, s10, 26
	s_load_dwordx16 s[4:19], s[0:1], 0x0
	s_waitcnt lgkmcnt(0)
	v_writelane_b32 v253, s4, 27
	s_nop 1
	v_writelane_b32 v253, s5, 28
	v_writelane_b32 v253, s6, 29
	v_writelane_b32 v253, s7, 30
	v_writelane_b32 v253, s8, 31
	v_writelane_b32 v253, s9, 32
	v_writelane_b32 v253, s10, 33
	v_writelane_b32 v253, s11, 34
	v_writelane_b32 v253, s12, 35
	v_writelane_b32 v253, s13, 36
	v_writelane_b32 v253, s14, 37
	v_writelane_b32 v253, s15, 38
	v_writelane_b32 v253, s16, 39
	v_writelane_b32 v253, s17, 40
	v_writelane_b32 v253, s18, 41
	v_writelane_b32 v253, s19, 42
	s_load_dwordx16 s[4:19], s[0:1], 0x40
	s_waitcnt lgkmcnt(0)
	v_writelane_b32 v253, s4, 43
	s_nop 1
	v_writelane_b32 v253, s5, 44
	v_writelane_b32 v253, s6, 45
	v_writelane_b32 v253, s7, 46
	v_writelane_b32 v253, s8, 47
	v_writelane_b32 v253, s9, 48
	v_writelane_b32 v253, s10, 49
	v_writelane_b32 v253, s11, 50
	v_writelane_b32 v253, s12, 51
	v_writelane_b32 v253, s13, 52
	v_writelane_b32 v253, s14, 53
	v_writelane_b32 v253, s15, 54
	v_writelane_b32 v253, s16, 55
	v_writelane_b32 v253, s17, 56
	v_writelane_b32 v253, s18, 57
	v_writelane_b32 v253, s19, 58
	s_load_dwordx2 s[6:7], s[0:1], 0x110
	s_waitcnt lgkmcnt(0)
	s_cmp_gt_i32 s6, 0
	s_cselect_b64 s[2:3], -1, 0
	s_cmp_lt_i32 s7, 1
	s_cselect_b64 s[4:5], -1, 0
	s_or_b64 s[2:3], s[2:3], s[4:5]
	s_and_b64 vcc, exec, s[2:3]
	s_cbranch_vccnz .LBB0_267
	s_mov_b32 s101, 0
.Lp0_body:
	s_cmp_lg_u32 s101, 0
	s_cbranch_scc1 .Lp0_sections
	v_readlane_b32 s39, v253, 3
	s_nop 3
	s_and_b32 s2, s39, 1
	s_cbranch_scc0 .Lp0_sections
	s_mov_b32 s101, 1
	v_mbcnt_lo_u32_b32 v99, -1, 0
	v_mbcnt_hi_u32_b32 v99, -1, v99
	v_readlane_b32 s1, v253, 20
	v_readlane_b32 s78, v253, 2
	s_nop 3
	s_lshl_b32 s0, s39, 3
	s_add_i32 s16, s0, s1
	s_lshl_b32 s8, s1, 14
	s_lshl_b32 s17, s78, 3
	v_lshlrev_b32_e32 v164, 3, v99
	v_ashrrev_i32_e32 v45, 3, v99
	v_and_b32_e32 v2, 7, v99
	v_mov_b32_e32 v33, 0
	v_ashrrev_i32_e32 v38, 3, v99
	v_lshlrev_b32_e32 v32, 2, v2
	v_and_b32_e32 v44, 24, v164
	v_lshlrev_b32_e32 v131, 11, v2
	v_lshlrev_b32_e32 v34, 4, v2
	v_mov_b32_e32 v35, v33
	s_branch .LBB0_205
.Lp0_sections:
	v_readlane_b32 s2, v253, 26
	s_andn2_b32 s2, s2, 63
	v_mbcnt_lo_u32_b32 v99, -1, 0
	v_mbcnt_hi_u32_b32 v99, -1, v99
	s_nop 0
	v_add_u32_e32 v96, s2, v99
	s_movk_i32 s2, 0x1000
	v_cmp_gt_i32_e64 s[84:85], s2, v96
	s_and_saveexec_b64 s[4:5], s[84:85]
	s_cbranch_execz .LBB0_19
	s_load_dwordx16 s[8:23], s[0:1], 0x0
	v_readlane_b32 s2, v253, 20
	s_lshl_b32 s2, s2, 8
	s_add_i32 s2, s2, 0
	v_ashrrev_i32_e32 v97, 31, v96
	s_waitcnt lgkmcnt(0)
	v_mov_b32_e32 v0, s10
	v_mov_b32_e32 v1, s11
	v_add_u32_e32 v2, 0xfffffe00, v96
	v_lshl_add_u32 v3, v99, 2, s2
	v_lshl_add_u64 v[0:1], v[96:97], 2, v[0:1]
	s_mov_b64 s[6:7], 0
	s_mov_b64 s[8:9], 0x800
	s_movk_i32 s10, 0xdff

.LBB0_205:
	s_cmp_eq_u32 s101, 2
	s_cbranch_scc1 .Lp0_end
	s_cmp_lt_i32 s16, 0x12000
	s_cselect_b64 s[0:1], -1, 0
	s_and_b64 vcc, exec, s[0:1]
	s_cbranch_vccz .LBB0_217
	s_add_i32 s2, s16, 0x4000
	s_cmp_lt_i32 s16, 0xc000
	s_cselect_b32 s2, s16, s2
	s_and_b64 s[0:1], exec, s[0:1]
	s_cselect_b32 s5, s2, 0
	s_ashr_i32 s0, s5, 31
	s_lshr_b32 s0, s0, 23
	s_add_i32 s6, s5, s0
	s_and_b32 s0, s6, 0xfffffe00
	s_sub_i32 s2, s5, s0
	s_and_b32 s3, s5, 0xff
	s_cmp_gt_i32 s5, 0xffff
	s_cselect_b64 s[0:1], -1, 0
	s_movk_i32 s4, 0x400
	s_and_b64 s[0:1], s[0:1], exec
	s_cselect_b32 s22, s4, 0x800
	s_cselect_b32 s0, s3, s2
	s_cselect_b32 s9, 10, 11
	s_lshr_b32 s4, s22, 5
	s_sext_i32_i16 s7, s4
	v_cvt_f32_i32_e32 v0, s7
	s_sext_i32_i16 s10, s0
	v_cvt_f32_i32_e32 v1, s10
	s_xor_b32 s7, s10, s7
	v_rcp_iflag_f32_e32 v2, v0
	s_ashr_i32 s7, s7, 30
	s_or_b32 s7, s7, 1
	s_mov_b32 s1, 0
	v_mul_f32_e32 v2, v1, v2
	v_trunc_f32_e32 v2, v2
	v_fma_f32 v1, -v2, v0, v1
	v_cvt_i32_f32_e32 v2, v2
	v_cmp_ge_f32_e64 s[2:3], |v1|, |v0|
	s_and_b64 s[2:3], s[2:3], exec
	s_cselect_b32 s2, s7, 0
	v_readfirstlane_b32 s3, v2
	s_add_i32 s14, s3, s2
	s_mul_i32 s2, s14, s4
	s_sub_i32 s0, s0, s2
	s_sext_i32_i16 s0, s0
	s_lshl_b32 s2, s0, 6
	s_lshl_b32 s4, s0, 5
	s_and_b32 s2, s2, 0x700
	s_cmp_gt_i32 s0, 31
	s_cselect_b32 s0, 0x80, 0
	s_or_b32 s0, s2, s0
	s_and_b32 s2, s4, 0x60
	s_or_b32 s0, s0, s2
	s_cmp_gt_i32 s5, 0xffff
	s_cselect_b64 s[2:3], -1, 0
	s_mov_b32 s7, 0x27600000
	s_and_b64 s[2:3], s[2:3], exec
	s_cselect_b32 s15, s7, 0x7600000
	s_cselect_b32 s23, s4, s0
	s_ashr_i32 s2, s6, 9
	s_add_i32 s0, s5, 0xffff0000
	s_ashr_i32 s3, s2, 31
	s_lshr_b32 s0, s0, 8
	s_lshl_b64 s[6:7], s[2:3], 21
	s_lshl_b64 s[10:11], s[0:1], 20
	s_cmp_gt_i32 s5, 0xffff
	s_cselect_b64 s[12:13], -1, 0
	s_and_b64 s[12:13], s[12:13], exec
	v_readlane_b32 s36, v253, 4
	s_cselect_b32 s6, s10, s6
	s_cselect_b32 s7, s11, s7
	s_lshl_b64 s[2:3], s[2:3], 23
	v_readlane_b32 s44, v253, 12
	v_readlane_b32 s45, v253, 13
	s_add_u32 s10, s44, s2
	v_readlane_b32 s48, v253, 16
	s_addc_u32 s11, s45, s3
	s_lshl_b64 s[2:3], s[0:1], 22
	v_readlane_b32 s49, v253, 17
	s_add_u32 s0, s48, s2
	s_addc_u32 s12, s49, s3
	s_cmp_gt_i32 s5, 0xffff
	s_cselect_b64 vcc, -1, 0
	s_and_b64 s[2:3], vcc, exec
	s_cselect_b32 s3, s12, s11
	s_cselect_b32 s2, s0, s10
	s_add_u32 s18, s94, 0x7600000
	s_addc_u32 s19, s95, 0
	s_add_u32 s20, s94, 0x27600000
	s_sext_i32_i16 s0, s14
	s_addc_u32 s21, s95, 0
	s_lshl_b32 s24, s0, 7
	s_add_u32 s0, s94, s15
	s_addc_u32 s5, s95, 0
	s_add_u32 s6, s0, s6
	s_addc_u32 s7, s5, s7
	v_add_u32_e32 v24, s24, v38
	s_ashr_i32 s5, s4, 31
	v_mov_b32_e32 v0, 0x43800000
	v_bfrev_b32_e32 v1, 34
	s_lshl_b64 s[10:11], s[4:5], 2
	v_ashrrev_i32_e32 v25, 31, v24
	v_cndmask_b32_e32 v41, v0, v1, vcc
	s_add_u32 s10, s2, s10
	v_lshlrev_b64 v[0:1], s9, v[24:25]
	v_add_u32_e32 v2, 8, v24
	v_add_u32_e32 v8, 16, v24
	v_add_u32_e32 v10, 24, v24
	v_add_u32_e32 v16, 32, v24
	v_add_u32_e32 v18, 40, v24
	v_add_u32_e32 v28, 48, v24
	v_add_u32_e32 v24, 56, v24
	s_addc_u32 s11, s3, s11
	v_ashrrev_i32_e32 v3, 31, v2
	v_ashrrev_i32_e32 v9, 31, v8
	v_ashrrev_i32_e32 v11, 31, v10
	v_ashrrev_i32_e32 v17, 31, v16
	v_ashrrev_i32_e32 v19, 31, v18
	v_ashrrev_i32_e32 v29, 31, v28
	v_ashrrev_i32_e32 v25, 31, v24
	v_lshl_add_u64 v[26:27], v[32:33], 2, s[10:11]
	v_lshlrev_b64 v[2:3], s9, v[2:3]
	v_lshlrev_b64 v[8:9], s9, v[8:9]
	v_lshlrev_b64 v[10:11], s9, v[10:11]
	v_lshlrev_b64 v[16:17], s9, v[16:17]
	v_lshlrev_b64 v[18:19], s9, v[18:19]
	v_lshlrev_b64 v[28:29], s9, v[28:29]
	v_lshlrev_b64 v[24:25], s9, v[24:25]
	v_lshl_add_u64 v[0:1], v[0:1], 2, v[26:27]
	v_lshl_add_u64 v[4:5], v[2:3], 2, v[26:27]
	v_lshl_add_u64 v[8:9], v[8:9], 2, v[26:27]
	v_lshl_add_u64 v[12:13], v[10:11], 2, v[26:27]
	v_lshl_add_u64 v[16:17], v[16:17], 2, v[26:27]
	v_lshl_add_u64 v[20:21], v[18:19], 2, v[26:27]
	v_lshl_add_u64 v[28:29], v[28:29], 2, v[26:27]
	v_lshl_add_u64 v[30:31], v[24:25], 2, v[26:27]
	global_load_dwordx4 v[0:3], v[0:1], off nt
	s_nop 0
	global_load_dwordx4 v[4:7], v[4:5], off nt
	s_nop 0
	global_load_dwordx4 v[8:11], v[8:9], off nt
	s_nop 0
	global_load_dwordx4 v[12:15], v[12:13], off nt
	s_nop 0
	global_load_dwordx4 v[16:19], v[16:17], off nt
	s_nop 0
	global_load_dwordx4 v[20:23], v[20:21], off nt
	s_nop 0
	global_load_dwordx4 v[24:27], v[28:29], off nt
	s_nop 0
	global_load_dwordx4 v[28:31], v[30:31], off nt
	v_lshrrev_b32_e32 v42, 1, v38
	v_or_b32_e32 v36, 3, v32
	v_or_b32_e32 v37, 2, v32
	v_or_b32_e32 v104, 1, v32
	v_and_b32_e32 v106, 7, v38
	v_and_b32_e32 v47, 24, v42
	v_bitop3_b32 v42, v47, v32, v106 bitop3:0x36
	v_bitop3_b32 v43, v47, v104, v106 bitop3:0x36
	v_bitop3_b32 v45, v47, v37, v106 bitop3:0x36
	v_bitop3_b32 v47, v47, v36, v106 bitop3:0x36
	v_lshlrev_b32_e32 v78, 2, v47
	v_add_u32_e32 v47, 8, v38
	v_lshl_add_u32 v50, v47, 7, s8
	v_lshrrev_b32_e32 v47, 1, v47
	v_and_b32_e32 v51, 24, v47
	v_bitop3_b32 v47, v51, v32, v106 bitop3:0x36
	v_bitop3_b32 v48, v51, v104, v106 bitop3:0x36
	v_bitop3_b32 v49, v51, v37, v106 bitop3:0x36
	v_bitop3_b32 v51, v51, v36, v106 bitop3:0x36
	v_lshl_add_u32 v47, v47, 2, v50
	v_lshl_add_u32 v48, v48, 2, v50
	v_lshl_add_u32 v49, v49, 2, v50
	v_lshl_add_u32 v50, v51, 2, v50
	v_add_u32_e32 v51, 16, v38
	v_lshl_add_u32 v54, v51, 7, s8
	v_lshrrev_b32_e32 v51, 1, v51
	v_and_b32_e32 v55, 24, v51
	v_bitop3_b32 v51, v55, v32, v106 bitop3:0x36
	v_bitop3_b32 v52, v55, v104, v106 bitop3:0x36
	v_bitop3_b32 v53, v55, v37, v106 bitop3:0x36
	v_bitop3_b32 v55, v55, v36, v106 bitop3:0x36
	v_lshl_add_u32 v51, v51, 2, v54
	v_lshl_add_u32 v52, v52, 2, v54
	v_lshl_add_u32 v53, v53, 2, v54
	v_lshl_add_u32 v54, v55, 2, v54
	v_add_u32_e32 v55, 24, v38
	v_lshl_add_u32 v58, v55, 7, s8
	v_lshrrev_b32_e32 v55, 1, v55
	v_and_b32_e32 v59, 24, v55
	v_bitop3_b32 v55, v59, v32, v106 bitop3:0x36
	v_bitop3_b32 v56, v59, v104, v106 bitop3:0x36
	v_bitop3_b32 v57, v59, v37, v106 bitop3:0x36
	v_bitop3_b32 v59, v59, v36, v106 bitop3:0x36
	v_lshl_add_u32 v55, v55, 2, v58
	v_lshl_add_u32 v56, v56, 2, v58
	v_lshl_add_u32 v57, v57, 2, v58
	v_lshl_add_u32 v58, v59, 2, v58
	v_add_u32_e32 v59, 32, v38
	v_lshl_add_u32 v62, v59, 7, s8
	v_lshrrev_b32_e32 v59, 1, v59
	v_and_b32_e32 v63, 24, v59
	v_bitop3_b32 v59, v63, v32, v106 bitop3:0x36
	v_bitop3_b32 v60, v63, v104, v106 bitop3:0x36
	v_bitop3_b32 v61, v63, v37, v106 bitop3:0x36
	v_bitop3_b32 v63, v63, v36, v106 bitop3:0x36
	v_lshl_add_u32 v59, v59, 2, v62
	v_lshl_add_u32 v60, v60, 2, v62
	v_lshl_add_u32 v61, v61, 2, v62
	v_lshl_add_u32 v62, v63, 2, v62
	v_add_u32_e32 v63, 40, v38
	v_lshl_add_u32 v66, v63, 7, s8
	v_lshrrev_b32_e32 v63, 1, v63
	v_and_b32_e32 v67, 24, v63
	v_bitop3_b32 v63, v67, v32, v106 bitop3:0x36
	v_bitop3_b32 v64, v67, v104, v106 bitop3:0x36
	v_bitop3_b32 v65, v67, v37, v106 bitop3:0x36
	v_bitop3_b32 v67, v67, v36, v106 bitop3:0x36
	v_lshl_add_u32 v63, v63, 2, v66
	v_lshl_add_u32 v64, v64, 2, v66
	v_lshl_add_u32 v65, v65, 2, v66
	v_lshl_add_u32 v66, v67, 2, v66
	v_add_u32_e32 v67, 48, v38
	v_lshl_add_u32 v70, v67, 7, s8
	v_lshrrev_b32_e32 v67, 1, v67
	v_and_b32_e32 v71, 24, v67
	v_bitop3_b32 v67, v71, v32, v106 bitop3:0x36
	v_bitop3_b32 v68, v71, v104, v106 bitop3:0x36
	v_bitop3_b32 v69, v71, v37, v106 bitop3:0x36
	v_bitop3_b32 v71, v71, v36, v106 bitop3:0x36
	v_lshl_add_u32 v67, v67, 2, v70
	v_lshl_add_u32 v68, v68, 2, v70
	v_lshl_add_u32 v69, v69, 2, v70
	v_lshl_add_u32 v70, v71, 2, v70
	v_add_u32_e32 v71, 56, v38
	v_lshl_add_u32 v74, v71, 7, s8
	v_lshrrev_b32_e32 v71, 1, v71
	v_and_b32_e32 v79, 24, v71
	v_add_u32_e32 v39, 64, v38
	v_bitop3_b32 v71, v79, v32, v106 bitop3:0x36
	v_bitop3_b32 v72, v79, v104, v106 bitop3:0x36
	v_bitop3_b32 v73, v79, v37, v106 bitop3:0x36
	v_bitop3_b32 v79, v79, v36, v106 bitop3:0x36
	v_lshl_add_u32 v46, v38, 7, s8
	v_lshlrev_b32_e32 v75, 2, v42
	v_lshlrev_b32_e32 v76, 2, v43
	v_lshlrev_b32_e32 v77, 2, v45
	v_lshl_add_u32 v71, v71, 2, v74
	v_lshl_add_u32 v72, v72, 2, v74
	v_lshl_add_u32 v73, v73, 2, v74
	v_lshl_add_u32 v74, v79, 2, v74
	v_lshl_add_u32 v79, v39, 7, s8
	v_add_u32_e32 v42, v46, v75
	v_add_u32_e32 v43, v46, v76
	v_add_u32_e32 v45, v46, v77
	v_add_u32_e32 v46, v46, v78
	v_add_u32_e32 v75, v79, v75
	v_add_u32_e32 v76, v79, v76
	v_add_u32_e32 v77, v79, v77
	v_add_u32_e32 v78, v79, v78
	v_add_u32_e32 v79, 0x48, v38
	v_lshl_add_u32 v82, v79, 7, s8
	v_lshrrev_b32_e32 v79, 1, v79
	v_and_b32_e32 v83, 24, v79
	v_bitop3_b32 v79, v83, v32, v106 bitop3:0x36
	v_bitop3_b32 v80, v83, v104, v106 bitop3:0x36
	v_bitop3_b32 v81, v83, v37, v106 bitop3:0x36
	v_bitop3_b32 v83, v83, v36, v106 bitop3:0x36
	v_lshl_add_u32 v79, v79, 2, v82
	v_lshl_add_u32 v80, v80, 2, v82
	v_lshl_add_u32 v81, v81, 2, v82
	v_lshl_add_u32 v82, v83, 2, v82
	v_add_u32_e32 v83, 0x50, v38
	v_lshl_add_u32 v86, v83, 7, s8
	v_lshrrev_b32_e32 v83, 1, v83
	v_and_b32_e32 v87, 24, v83
	v_bitop3_b32 v83, v87, v32, v106 bitop3:0x36
	v_bitop3_b32 v84, v87, v104, v106 bitop3:0x36
	v_bitop3_b32 v85, v87, v37, v106 bitop3:0x36
	v_bitop3_b32 v87, v87, v36, v106 bitop3:0x36
	v_lshl_add_u32 v83, v83, 2, v86
	v_lshl_add_u32 v84, v84, 2, v86
	v_lshl_add_u32 v85, v85, 2, v86
	v_lshl_add_u32 v86, v87, 2, v86
	v_add_u32_e32 v87, 0x58, v38
	v_lshl_add_u32 v90, v87, 7, s8
	v_lshrrev_b32_e32 v87, 1, v87
	v_and_b32_e32 v91, 24, v87
	v_bitop3_b32 v87, v91, v32, v106 bitop3:0x36
	v_bitop3_b32 v88, v91, v104, v106 bitop3:0x36
	v_bitop3_b32 v89, v91, v37, v106 bitop3:0x36
	v_bitop3_b32 v91, v91, v36, v106 bitop3:0x36
	v_lshl_add_u32 v87, v87, 2, v90
	v_lshl_add_u32 v88, v88, 2, v90
	v_lshl_add_u32 v89, v89, 2, v90
	v_lshl_add_u32 v90, v91, 2, v90
	v_add_u32_e32 v91, 0x60, v38
	v_lshl_add_u32 v94, v91, 7, s8
	v_lshrrev_b32_e32 v91, 1, v91
	v_and_b32_e32 v95, 24, v91
	v_bitop3_b32 v91, v95, v32, v106 bitop3:0x36
	v_bitop3_b32 v92, v95, v104, v106 bitop3:0x36
	v_bitop3_b32 v93, v95, v37, v106 bitop3:0x36
	v_bitop3_b32 v95, v95, v36, v106 bitop3:0x36
	v_lshl_add_u32 v91, v91, 2, v94
	v_lshl_add_u32 v92, v92, 2, v94
	v_lshl_add_u32 v93, v93, 2, v94
	v_lshl_add_u32 v94, v95, 2, v94
	v_add_u32_e32 v95, 0x68, v38
	v_lshl_add_u32 v98, v95, 7, s8
	v_lshrrev_b32_e32 v95, 1, v95
	v_and_b32_e32 v99, 24, v95
	v_bitop3_b32 v95, v99, v32, v106 bitop3:0x36
	v_bitop3_b32 v96, v99, v104, v106 bitop3:0x36
	v_bitop3_b32 v97, v99, v37, v106 bitop3:0x36
	v_bitop3_b32 v99, v99, v36, v106 bitop3:0x36
	v_lshl_add_u32 v95, v95, 2, v98
	v_lshl_add_u32 v96, v96, 2, v98
	v_lshl_add_u32 v97, v97, 2, v98
	v_lshl_add_u32 v98, v99, 2, v98
	v_add_u32_e32 v99, 0x70, v38
	v_lshl_add_u32 v102, v99, 7, s8
	v_lshrrev_b32_e32 v99, 1, v99
	v_and_b32_e32 v103, 24, v99
	v_bitop3_b32 v99, v103, v32, v106 bitop3:0x36
	v_bitop3_b32 v100, v103, v104, v106 bitop3:0x36
	v_bitop3_b32 v101, v103, v37, v106 bitop3:0x36
	v_bitop3_b32 v103, v103, v36, v106 bitop3:0x36
	v_lshl_add_u32 v99, v99, 2, v102
	v_lshl_add_u32 v100, v100, 2, v102
	v_lshl_add_u32 v101, v101, 2, v102
	v_lshl_add_u32 v102, v103, 2, v102
	v_add_u32_e32 v103, 0x78, v38
	v_lshl_add_u32 v107, v103, 7, s8
	v_lshrrev_b32_e32 v103, 1, v103
	v_and_b32_e32 v108, 24, v103
	v_bitop3_b32 v103, v108, v32, v106 bitop3:0x36
	v_bitop3_b32 v104, v108, v104, v106 bitop3:0x36
	v_bitop3_b32 v37, v108, v37, v106 bitop3:0x36
	v_bitop3_b32 v36, v108, v36, v106 bitop3:0x36
	v_add_u32_e32 v40, s8, v131
	v_lshl_add_u32 v103, v103, 2, v107
	v_lshl_add_u32 v104, v104, 2, v107
	v_lshl_add_u32 v105, v37, 2, v107
	v_lshl_add_u32 v106, v36, 2, v107
	v_or_b32_e32 v107, 1, v44
	v_or_b32_e32 v108, 2, v44
	v_or_b32_e32 v109, 3, v44
	v_or_b32_e32 v110, 4, v44
	v_or_b32_e32 v111, 5, v44
	v_or_b32_e32 v112, 6, v44
	v_or_b32_e32 v113, 7, v44
	s_mov_b32 s25, 0xc3e00000
	v_mov_b32_e32 v37, 0
	v_mov_b32_e32 v114, 0x43e00000
	v_readlane_b32 s37, v253, 5
	v_readlane_b32 s38, v253, 6
	v_readlane_b32 s39, v253, 7
	v_readlane_b32 s40, v253, 8
	v_readlane_b32 s41, v253, 9
	v_readlane_b32 s42, v253, 10
	v_readlane_b32 s43, v253, 11
	v_readlane_b32 s46, v253, 14
	v_readlane_b32 s47, v253, 15
	v_readlane_b32 s50, v253, 18
	v_readlane_b32 s51, v253, 19

.LBB0_217:
	s_cmp_eq_u32 s101, 1
	s_cbranch_scc0 .Lp0_end
	s_mov_b32 s101, 2
	s_waitcnt vmcnt(0) lgkmcnt(0)
	s_barrier
	v_readlane_b32 s0, v253, 0
	v_readlane_b32 s1, v253, 1
	s_nop 3
	s_sub_u32 s0, s0, 0x118
	s_subb_u32 s1, s1, 0
	s_branch .Lp0_body
